# ROW_MIX l1-3 and ROW_FINAL row loops: next-row prefetch loads no longer waited right after issue; counted wait moved to latch end
# speedup vs baseline: 1.0258x; 1.0098x over previous
.LBB0_1131:
	v_lshlrev_b32_e32 v128, 16, v112
	v_and_b32_e32 v129, 0xffff0000, v112
	v_lshlrev_b32_e32 v130, 16, v110
	v_and_b32_e32 v131, 0xffff0000, v110
	v_lshlrev_b32_e32 v112, 16, v113
	v_and_b32_e32 v113, 0xffff0000, v113
	v_lshlrev_b32_e32 v110, 16, v111
	v_and_b32_e32 v111, 0xffff0000, v111
	v_pk_fma_f32 v[2:3], v[54:55], v[2:3], v[128:129]
	v_pk_fma_f32 v[6:7], v[50:51], v[6:7], v[130:131]
	v_pk_fma_f32 v[4:5], v[56:57], v[4:5], v[112:113]
	v_cvt_pk_bf16_f32 v2, v2, v3
	v_pk_fma_f32 v[8:9], v[52:53], v[8:9], v[110:111]
	v_cvt_pk_bf16_f32 v6, v6, v7
	v_cvt_pk_bf16_f32 v3, v4, v5
	v_and_b32_e32 v5, 0xffff0000, v2
	v_cvt_pk_bf16_f32 v7, v8, v9
	v_and_b32_e32 v9, 0xffff0000, v6
	v_lshlrev_b32_e32 v132, 16, v108
	v_and_b32_e32 v133, 0xffff0000, v108
	v_lshlrev_b32_e32 v4, 16, v2
	v_lshlrev_b32_e32 v8, 16, v6
	v_mul_f32_e32 v0, v5, v5
	v_mul_f32_e32 v95, v9, v9
	v_lshlrev_b32_e32 v108, 16, v109
	v_and_b32_e32 v109, 0xffff0000, v109
	v_lshlrev_b32_e32 v112, 16, v3
	v_lshlrev_b32_e32 v110, 16, v7
	v_pk_fma_f32 v[10:11], v[58:59], v[10:11], v[132:133]
	v_fmac_f32_e32 v0, v4, v4
	v_fmac_f32_e32 v95, v8, v8
	v_and_b32_e32 v113, 0xffff0000, v3
	v_and_b32_e32 v111, 0xffff0000, v7
	v_pk_fma_f32 v[12:13], v[60:61], v[12:13], v[108:109]
	v_cvt_pk_bf16_f32 v10, v10, v11
	v_fmac_f32_e32 v0, v112, v112
	v_fmac_f32_e32 v95, v110, v110
	v_cvt_pk_bf16_f32 v11, v12, v13
	v_and_b32_e32 v13, 0xffff0000, v10
	v_fmac_f32_e32 v0, v113, v113
	v_fmac_f32_e32 v95, v111, v111
	v_lshlrev_b32_e32 v134, 16, v104
	v_and_b32_e32 v135, 0xffff0000, v104
	v_lshlrev_b32_e32 v12, 16, v10
	v_add_f32_e32 v0, v95, v0
	v_mul_f32_e32 v95, v13, v13
	v_lshlrev_b32_e32 v104, 16, v105
	v_and_b32_e32 v105, 0xffff0000, v105
	v_lshlrev_b32_e32 v108, 16, v11
	v_pk_fma_f32 v[14:15], v[62:63], v[14:15], v[134:135]
	v_fmac_f32_e32 v95, v12, v12
	v_and_b32_e32 v109, 0xffff0000, v11
	v_pk_fma_f32 v[16:17], v[64:65], v[16:17], v[104:105]
	v_cvt_pk_bf16_f32 v14, v14, v15
	v_fmac_f32_e32 v95, v108, v108
	v_cvt_pk_bf16_f32 v15, v16, v17
	v_and_b32_e32 v17, 0xffff0000, v14
	v_fmac_f32_e32 v95, v109, v109
	v_lshlrev_b32_e32 v16, 16, v14
	v_add_f32_e32 v0, v95, v0
	v_mul_f32_e32 v95, v17, v17
	v_lshlrev_b32_e32 v104, 16, v15
	v_fmac_f32_e32 v95, v16, v16
	v_and_b32_e32 v105, 0xffff0000, v15
	v_fmac_f32_e32 v95, v104, v104
	v_fmac_f32_e32 v95, v105, v105
	v_add_f32_e32 v0, v95, v0
	v_lshlrev_b64 v[84:85], 11, v[84:85]
	v_lshl_add_u64 v[128:129], v[86:87], 0, v[84:85]
	v_add_f32_dpp v0, v0, v0 quad_perm:[1,0,3,2] row_mask:0xf bank_mask:0xf bound_ctrl:1
	global_store_dwordx2 v[128:129], v[2:3], off
	global_store_dwordx2 v[128:129], v[6:7], off offset:512
	global_store_dwordx2 v[128:129], v[10:11], off offset:1024
	global_store_dwordx2 v[128:129], v[14:15], off offset:1536
	v_add_f32_dpp v0, v0, v0 quad_perm:[2,3,0,1] row_mask:0xf bank_mask:0xf bound_ctrl:1
	v_mov_b32_e32 v126, v127
	v_add_f32_dpp v0, v0, v0 row_half_mirror row_mask:0xf bank_mask:0xf bound_ctrl:1
	s_nop 1
	v_add_f32_dpp v0, v0, v0 row_mirror row_mask:0xf bank_mask:0xf bound_ctrl:1
	s_nop 0
	v_readlane_b32 s6, v0, 16
	v_readlane_b32 s2, v0, 0
	s_nop 0
	v_mov_b32_e32 v95, s6
	v_add_f32_e32 v95, s2, v95
	v_readlane_b32 s2, v0, 32
	s_nop 1
	v_add_f32_e32 v95, s2, v95
	v_readlane_b32 s2, v0, 48
	s_nop 1
	v_add_f32_e32 v0, s2, v95
	v_fmamk_f32 v0, v0, 0x3a800000, v83
	v_mul_f32_e32 v95, 0x4f800000, v0
	v_cmp_gt_f32_e32 vcc, s22, v0
	s_nop 1
	v_cndmask_b32_e32 v0, v0, v95, vcc
	v_sqrt_f32_e32 v95, v0
	s_nop 0
	v_add_u32_e32 v2, -1, v95
	v_fma_f32 v3, -v2, v95, v0
	v_cmp_ge_f32_e64 s[6:7], 0, v3
	v_add_u32_e32 v3, 1, v95
	s_nop 0
	v_cndmask_b32_e64 v2, v95, v2, s[6:7]
	v_fma_f32 v95, -v3, v95, v0
	v_cmp_lt_f32_e64 s[6:7], 0, v95
	s_nop 1
	v_cndmask_b32_e64 v2, v2, v3, s[6:7]
	v_mul_f32_e32 v3, 0x37800000, v2
	v_cndmask_b32_e32 v2, v2, v3, vcc
	v_cmp_class_f32_e32 vcc, v0, v117
	s_nop 1
	v_cndmask_b32_e32 v0, v2, v0, vcc
	v_div_scale_f32 v2, s[6:7], v0, v0, 1.0
	v_rcp_f32_e32 v3, v2
	s_nop 0
	v_fma_f32 v6, -v2, v3, 1.0
	v_fmac_f32_e32 v3, v6, v3
	v_div_scale_f32 v6, vcc, 1.0, v0, 1.0
	v_mul_f32_e32 v7, v6, v3
	v_fma_f32 v10, -v2, v7, v6
	v_fmac_f32_e32 v7, v10, v3
	v_fma_f32 v2, -v2, v7, v6
	v_div_fmas_f32 v2, v2, v3, v7
	v_div_fixup_f32 v0, v2, v0, 1.0
	v_pk_mul_f32 v[2:3], v[0:1], v[112:113] op_sel_hi:[0,1]
	v_pk_mul_f32 v[4:5], v[0:1], v[4:5] op_sel_hi:[0,1]
	v_pk_mul_f32 v[4:5], v[26:27], v[4:5]
	v_pk_mul_f32 v[2:3], v[28:29], v[2:3]
	v_pk_fma_f32 v[4:5], v[66:67], v[4:5], v[38:39]
	v_pk_fma_f32 v[2:3], v[68:69], v[2:3], v[40:41]
	v_cvt_pk_bf16_f32 v4, v4, v5
	v_cvt_pk_bf16_f32 v5, v2, v3
	v_lshl_add_u64 v[2:3], v[92:93], 0, v[84:85]
	global_store_dwordx2 v[2:3], v[4:5], off
	v_pk_mul_f32 v[4:5], v[0:1], v[110:111] op_sel_hi:[0,1]
	v_pk_mul_f32 v[6:7], v[0:1], v[8:9] op_sel_hi:[0,1]
	v_pk_mul_f32 v[6:7], v[18:19], v[6:7]
	v_pk_mul_f32 v[4:5], v[20:21], v[4:5]
	v_pk_fma_f32 v[6:7], v[70:71], v[6:7], v[34:35]
	v_pk_fma_f32 v[4:5], v[72:73], v[4:5], v[36:37]
	v_cvt_pk_bf16_f32 v6, v6, v7
	v_cvt_pk_bf16_f32 v7, v4, v5
	global_store_dwordx2 v[2:3], v[6:7], off offset:512
	v_pk_mul_f32 v[4:5], v[0:1], v[108:109] op_sel_hi:[0,1]
	v_pk_mul_f32 v[6:7], v[0:1], v[12:13] op_sel_hi:[0,1]
	v_pk_mul_f32 v[6:7], v[22:23], v[6:7]
	v_pk_mul_f32 v[4:5], v[24:25], v[4:5]
	v_pk_fma_f32 v[6:7], v[74:75], v[6:7], v[42:43]
	v_pk_fma_f32 v[4:5], v[76:77], v[4:5], v[44:45]
	v_cvt_pk_bf16_f32 v6, v6, v7
	v_cvt_pk_bf16_f32 v7, v4, v5
	global_store_dwordx2 v[2:3], v[6:7], off offset:1024
	v_pk_mul_f32 v[4:5], v[0:1], v[104:105] op_sel_hi:[0,1]
	v_pk_mul_f32 v[6:7], v[0:1], v[16:17] op_sel_hi:[0,1]
	v_pk_mul_f32 v[6:7], v[30:31], v[6:7]
	v_pk_mul_f32 v[4:5], v[32:33], v[4:5]
	v_pk_fma_f32 v[6:7], v[78:79], v[6:7], v[46:47]
	v_pk_fma_f32 v[4:5], v[80:81], v[4:5], v[48:49]
	v_cvt_pk_bf16_f32 v6, v6, v7
	v_cvt_pk_bf16_f32 v7, v4, v5
	global_store_dwordx2 v[2:3], v[6:7], off offset:1536
	s_waitcnt vmcnt(8)
	v_mov_b32_e32 v11, v124
	v_mov_b32_e32 v9, v123
	v_mov_b32_e32 v7, v122
	v_mov_b32_e32 v5, v121
	v_mov_b32_e32 v4, v120
	v_mov_b32_e32 v6, v119
	v_mov_b32_e32 v8, v118
	v_mov_b32_e32 v10, v97
	v_mov_b32_e32 v84, v96
	v_mov_b32_e32 v112, v106
	v_mov_b32_e32 v113, v107
	v_mov_b32_e32 v110, v102
	v_mov_b32_e32 v111, v103
	v_mov_b32_e32 v108, v100
	v_mov_b32_e32 v109, v101
	v_mov_b32_e32 v104, v98
	v_mov_b32_e32 v105, v99
	s_andn2_b64 exec, exec, s[4:5]
	s_cbranch_execz .LBB0_1145

.LBB0_1136:
	v_add_u32_e32 v2, 3, v84
	v_cmp_lt_i32_e64 s[6:7], v2, v114
	v_mov_b32_e32 v127, v115
	v_mov_b32_e32 v115, v116
	s_and_saveexec_b64 s[20:21], s[6:7]
	s_cbranch_execz .LBB0_1138
	v_ashrrev_i32_e32 v3, 31, v2
	v_lshlrev_b64 v[2:3], 6, v[2:3]
	v_lshl_add_u64 v[2:3], v[90:91], 0, v[2:3]
	global_load_dword v116, v[2:3], off

.LBB0_1139:
	s_or_b64 exec, exec, s[18:19]
	v_ashrrev_i32_e32 v85, 31, v84
	v_lshrrev_b32_e32 v0, 20, v85
	v_add_u32_e32 v0, v84, v0
	s_and_b64 s[6:7], exec, vcc
	v_ashrrev_i32_e32 v0, 12, v0
	v_cmp_gt_i32_e32 vcc, s17, v84
	s_or_b64 s[4:5], s[6:7], s[4:5]
	s_nop 0
	v_cndmask_b32_e32 v2, 8, v0, vcc
	v_cmp_ne_u32_e32 vcc, v2, v125
	s_and_saveexec_b64 s[6:7], vcc
	s_cbranch_execz .LBB0_1141
	v_mul_hi_i32_i24_e32 v13, 0x6000, v2
	v_mul_i32_i24_e32 v12, 0x6000, v2
	v_lshl_add_u64 v[12:13], s[8:9], 0, v[12:13]
	v_lshlrev_b32_e32 v0, 2, v82
	v_lshl_add_u64 v[16:17], v[12:13], 0, v[0:1]
	v_add_co_u32_e32 v48, vcc, 0x37000, v16
	v_lshl_add_u64 v[46:47], v[16:17], 0, s[10:11]
	s_nop 0
	v_addc_co_u32_e32 v49, vcc, 0, v17, vcc
	v_add_co_u32_e32 v38, vcc, 0x36000, v16
	v_lshl_add_u64 v[62:63], v[16:17], 0, s[14:15]
	s_nop 0
	v_addc_co_u32_e32 v39, vcc, 0, v17, vcc
	v_add_co_u32_e32 v16, vcc, 0x5000, v16
	global_load_dwordx4 v[12:15], v[48:49], off offset:1024
	global_load_dwordx4 v[74:77], v[48:49], off offset:2048
	global_load_dwordx4 v[34:37], v[46:47], off offset:1024
	global_load_dwordx4 v[42:45], v[46:47], off offset:2048
	s_nop 0
	global_load_dwordx4 v[38:41], v[38:39], off
	s_nop 0
	global_load_dwordx4 v[78:81], v[48:49], off offset:3072
	global_load_dwordx4 v[66:69], v[48:49], off
	s_nop 0
	global_load_dwordx4 v[46:49], v[46:47], off offset:3072
	v_addc_co_u32_e32 v17, vcc, 0, v17, vcc
	global_load_dwordx4 v[50:53], v[62:63], off offset:1024
	global_load_dwordx4 v[58:61], v[62:63], off offset:2048
	global_load_dwordx4 v[54:57], v[16:17], off
	s_nop 0
	global_load_dwordx4 v[62:65], v[62:63], off offset:3072
	v_mov_b32_e32 v125, v2
	s_waitcnt vmcnt(11)
	v_pk_add_f32 v[72:73], v[14:15], 1.0 op_sel_hi:[1,0]
	v_pk_add_f32 v[70:71], v[12:13], 1.0 op_sel_hi:[1,0]
	s_waitcnt vmcnt(10)
	v_pk_add_f32 v[76:77], v[76:77], 1.0 op_sel_hi:[1,0]
	v_pk_add_f32 v[74:75], v[74:75], 1.0 op_sel_hi:[1,0]
	s_waitcnt vmcnt(6)
	v_pk_add_f32 v[80:81], v[80:81], 1.0 op_sel_hi:[1,0]
	s_waitcnt vmcnt(5)
	v_pk_add_f32 v[68:69], v[68:69], 1.0 op_sel_hi:[1,0]
	v_pk_add_f32 v[66:67], v[66:67], 1.0 op_sel_hi:[1,0]
	v_pk_add_f32 v[78:79], v[78:79], 1.0 op_sel_hi:[1,0]
	s_waitcnt vmcnt(0)

.LBB0_1197:
	s_or_b64 exec, exec, s[0:1]
	v_readlane_b32 s2, v242, 1
	s_waitcnt lgkmcnt(0)
	s_barrier
	s_nop 0
	s_mov_b32 s0, 0
	v_readlane_b32 s3, v242, 2
	s_load_dwordx4 s[8:11], s[2:3], s0 offset:0xe8
	s_load_dwordx2 s[14:15], s[2:3], s0 offset:0xf8
	s_load_dwordx2 s[4:5], s[2:3], s0 offset:0x108
	v_cndmask_b32_e64 v0, 0, 1, s[12:13]
	v_mov_b32_e32 v140, v208
	v_cmp_ne_u32_e64 s[0:1], 1, v0
	s_andn2_b64 vcc, exec, s[12:13]
	v_readfirstlane_b32 s33, v140
	v_writelane_b32 v242, s0, 37
	s_nop 1
	v_writelane_b32 v242, s1, 38
	s_cbranch_vccnz .LBB0_1209
	v_lshlrev_b32_e32 v0, 4, v140
	v_add_u32_e32 v1, 0x2000, v0
	v_ashrrev_i32_e32 v2, 31, v1
	v_lshrrev_b32_e32 v2, 22, v2
	v_add_u32_e32 v2, v1, v2
	v_ashrrev_i32_e32 v2, 10, v2
	v_mul_i32_i24_e32 v3, 0x400, v2
	v_sub_u32_e32 v1, v1, v3
	v_lshrrev_b32_e32 v3, 4, v1
	v_bitop3_b32 v1, v3, v1, 32 bitop3:0x6c
	v_ashrrev_i32_e32 v3, 31, v1
	v_lshrrev_b32_e32 v3, 26, v3
	v_add_u32_e32 v3, v1, v3
	v_lshlrev_b32_e32 v5, 3, v2
	v_ashrrev_i32_e32 v4, 6, v3
	v_and_b32_e32 v5, -16, v5
	v_and_b32_e32 v3, 0xc0, v3
	v_add_u32_e32 v5, v4, v5
	v_sub_u32_e32 v1, v1, v3
	v_mov_b32_e32 v3, 1
	v_and_b32_e32 v4, 3, v4
	s_mov_b32 s0, 0x1fffe0
	v_lshrrev_b32_e32 v6, 2, v5
	v_lshlrev_b32_e32 v7, 1, v5
	v_lshlrev_b32_e32 v2, 5, v2
	v_ashrrev_i16_sdwa v1, v3, sext(v1) dst_sel:DWORD dst_unused:UNUSED_PAD src0_sel:DWORD src1_sel:BYTE_0
	v_and_or_b32 v4, v5, s0, v4
	v_and_b32_e32 v6, 4, v6
	v_and_b32_e32 v7, 24, v7
	v_and_b32_e32 v2, 32, v2
	v_bfe_i32 v1, v1, 0, 16
	v_or3_b32 v4, v4, v6, v7
	v_add_lshl_u32 v1, v2, v1, 1
	v_lshl_add_u32 v128, v4, 11, v1
	v_lshl_add_u32 v130, v5, 11, v1
	v_bfe_i32 v1, v140, 27, 1
	v_lshrrev_b32_e32 v1, 22, v1
	v_add_u32_e32 v1, v0, v1
	v_and_b32_e32 v1, 0xfffffc00, v1
	v_sub_u32_e32 v0, v0, v1
	v_lshrrev_b32_e32 v1, 4, v0
	v_ashrrev_i32_e32 v4, 31, v140
	v_bitop3_b32 v0, v1, v0, 32 bitop3:0x6c
	v_lshrrev_b32_e32 v4, 26, v4
	v_ashrrev_i32_e32 v1, 31, v0
	v_add_u32_e32 v4, v140, v4
	s_waitcnt lgkmcnt(0)
	s_add_u32 s38, s4, 0x1cef000
	v_lshrrev_b32_e32 v1, 26, v1
	v_ashrrev_i32_e32 v4, 6, v4
	s_addc_u32 s39, s5, 0
	v_add_u32_e32 v1, v0, v1
	v_lshlrev_b32_e32 v5, 3, v4
	s_add_u32 s40, s4, 0xdbff000
	v_ashrrev_i32_e32 v2, 6, v1
	v_and_b32_e32 v5, -16, v5
	v_readlane_b32 s2, v242, 0
	s_addc_u32 s41, s5, 0
	v_add_u32_e32 v5, v2, v5
	v_and_b32_e32 v2, 3, v2
	s_ashr_i32 s42, s2, 31
	v_and_or_b32 v2, v5, s0, v2
	s_lshr_b32 s0, s42, 29
	s_add_i32 s0, s2, s0
	s_ashr_i32 s7, s33, 6
	s_ashr_i32 s1, s0, 3
	s_and_b32 s0, s0, -8
	s_ashr_i32 s12, s33, 8
	s_lshl_b32 s13, s7, 10
	s_sub_i32 s0, s2, s0
	s_cmp_lt_i32 s0, 0
	s_movk_i32 s43, 0x89
	s_cselect_b32 s2, s43, 0x88
	s_mul_i32 s0, s2, s0
	s_add_i32 s0, s0, s1
	s_ashr_i32 s1, s0, 31
	s_lshr_b32 s1, s1, 26
	s_add_i32 s1, s0, s1
	s_ashr_i32 s2, s1, 6
	s_andn2_b32 s1, s1, 63
	s_sub_i32 s0, s0, s1
	s_bfe_i32 s1, s0, 0x80000
	s_bfe_u32 s1, s1, 0x3000c
	s_add_i32 s1, s0, s1
	s_bfe_i32 s3, s1, 0x80000
	s_and_b32 s1, s1, 0xf8
	s_sub_i32 s0, s0, s1
	s_lshl_b32 s2, s2, 3
	s_sext_i32_i16 s3, s3
	s_sext_i32_i8 s0, s0
	s_lshr_b32 s6, s3, 3
	s_add_i32 s2, s2, s0
	v_and_b32_e32 v1, 0xc0, v1
	s_ashr_i32 s3, s2, 31
	s_bfe_i64 s[16:17], s[6:7], 0x100000
	v_sub_u32_e32 v0, v0, v1
	s_lshl_b64 s[0:1], s[2:3], 19
	s_lshl_b64 s[16:17], s[16:17], 19
	v_lshrrev_b32_e32 v6, 2, v5
	v_lshlrev_b32_e32 v7, 1, v5
	v_lshlrev_b32_e32 v4, 5, v4
	v_ashrrev_i16_sdwa v0, v3, sext(v0) dst_sel:DWORD dst_unused:UNUSED_PAD src0_sel:DWORD src1_sel:BYTE_0
	s_add_u32 s16, s38, s16
	v_and_b32_e32 v6, 4, v6
	v_and_b32_e32 v7, 24, v7
	v_and_b32_e32 v4, 32, v4
	v_bfe_i32 v0, v0, 0, 16
	s_addc_u32 s17, s39, s17
	s_add_i32 s3, s13, 0
	v_or3_b32 v2, v2, v6, v7
	v_add_lshl_u32 v0, v4, v0, 1
	s_add_i32 s44, s3, 0x10000
	s_add_i32 s45, s3, 0x12000
	v_lshl_add_u32 v132, v2, 11, v0
	v_lshl_add_u32 v134, v5, 11, v0
	v_mov_b32_e32 v0, 0x7f
	s_mov_b64 s[18:19], s[16:17]
	s_mov_b32 m0, s44
	s_add_u32 s22, s40, s0
	s_addc_u32 s23, s41, s1
	global_load_lds_dwordx4 v132, s[18:19]
	s_mov_b32 m0, s45
	s_mov_b64 s[0:1], s[22:23]
	global_load_lds_dwordx4 v128, s[18:19]
	s_mov_b32 m0, s3
	s_add_i32 s46, s3, 0x2000
	v_mov_b32_e32 v133, 0
	global_load_lds_dwordx4 v134, s[0:1]
	s_mov_b32 m0, s46
	s_mov_b32 s51, 0
	global_load_lds_dwordx4 v130, s[0:1]
	s_add_u32 s0, s16, 0x40000
	s_addc_u32 s1, s17, 0
	s_add_i32 s47, s3, 0x14000
	s_mov_b32 m0, s47
	s_add_i32 s48, s3, 0x16000
	v_mov_b32_e32 v129, v133
	global_load_lds_dwordx4 v132, s[0:1]
	s_mov_b32 m0, s48
	v_mov_b32_e32 v135, v133
	global_load_lds_dwordx4 v128, s[0:1]
	s_add_u32 s0, s22, 0x40000
	s_addc_u32 s1, s23, 0
	s_add_i32 s49, s3, 0x4000
	s_mov_b32 m0, s49
	s_add_i32 s50, s3, 0x6000
	s_cmp_lg_u32 s12, 1
	global_load_lds_dwordx4 v134, s[0:1]
	s_mov_b32 m0, s50
	v_mov_b32_e32 v131, v133
	global_load_lds_dwordx4 v130, s[0:1]
	s_cbranch_scc1 .LBB0_1200
	s_barrier

.LBB0_2127:
	v_lshlrev_b32_e32 v130, 16, v94
	v_and_b32_e32 v131, 0xffff0000, v94
	v_lshlrev_b32_e32 v132, 16, v92
	v_and_b32_e32 v133, 0xffff0000, v92
	v_lshlrev_b32_e32 v94, 16, v95
	v_and_b32_e32 v95, 0xffff0000, v95
	v_lshlrev_b32_e32 v92, 16, v93
	v_and_b32_e32 v93, 0xffff0000, v93
	v_pk_fma_f32 v[110:111], v[36:37], v[110:111], v[130:131]
	v_pk_fma_f32 v[106:107], v[32:33], v[106:107], v[132:133]
	v_pk_fma_f32 v[94:95], v[38:39], v[112:113], v[94:95]
	v_cvt_pk_bf16_f32 v110, v110, v111
	v_pk_fma_f32 v[92:93], v[34:35], v[108:109], v[92:93]
	v_cvt_pk_bf16_f32 v106, v106, v107
	v_cvt_pk_bf16_f32 v111, v94, v95
	v_and_b32_e32 v95, 0xffff0000, v110
	v_cvt_pk_bf16_f32 v107, v92, v93
	v_and_b32_e32 v93, 0xffff0000, v106
	v_lshlrev_b32_e32 v134, 16, v90
	v_and_b32_e32 v135, 0xffff0000, v90
	v_lshlrev_b32_e32 v94, 16, v110
	v_lshlrev_b32_e32 v92, 16, v106
	v_mul_f32_e32 v79, v95, v95
	v_mul_f32_e32 v127, v93, v93
	v_lshlrev_b32_e32 v90, 16, v91
	v_and_b32_e32 v91, 0xffff0000, v91
	v_lshlrev_b32_e32 v112, 16, v111
	v_lshlrev_b32_e32 v108, 16, v107
	v_pk_fma_f32 v[102:103], v[40:41], v[102:103], v[134:135]
	v_fmac_f32_e32 v79, v94, v94
	v_fmac_f32_e32 v127, v92, v92
	v_and_b32_e32 v113, 0xffff0000, v111
	v_and_b32_e32 v109, 0xffff0000, v107
	v_pk_fma_f32 v[90:91], v[42:43], v[104:105], v[90:91]
	v_cvt_pk_bf16_f32 v102, v102, v103
	v_fmac_f32_e32 v79, v112, v112
	v_fmac_f32_e32 v127, v108, v108
	v_cvt_pk_bf16_f32 v103, v90, v91
	v_and_b32_e32 v91, 0xffff0000, v102
	v_fmac_f32_e32 v79, v113, v113
	v_fmac_f32_e32 v127, v109, v109
	v_lshlrev_b32_e32 v136, 16, v86
	v_and_b32_e32 v137, 0xffff0000, v86
	v_lshlrev_b32_e32 v90, 16, v102
	v_add_f32_e32 v79, v127, v79
	v_mul_f32_e32 v127, v91, v91
	v_lshlrev_b32_e32 v86, 16, v87
	v_and_b32_e32 v87, 0xffff0000, v87
	v_lshlrev_b32_e32 v104, 16, v103
	v_pk_fma_f32 v[98:99], v[44:45], v[98:99], v[136:137]
	v_fmac_f32_e32 v127, v90, v90
	v_and_b32_e32 v105, 0xffff0000, v103
	v_pk_fma_f32 v[86:87], v[46:47], v[100:101], v[86:87]
	v_cvt_pk_bf16_f32 v98, v98, v99
	v_fmac_f32_e32 v127, v104, v104
	v_cvt_pk_bf16_f32 v99, v86, v87
	v_and_b32_e32 v87, 0xffff0000, v98
	v_fmac_f32_e32 v127, v105, v105
	v_lshlrev_b32_e32 v86, 16, v98
	v_add_f32_e32 v79, v127, v79
	v_mul_f32_e32 v127, v87, v87
	v_lshlrev_b32_e32 v100, 16, v99
	v_fmac_f32_e32 v127, v86, v86
	v_and_b32_e32 v101, 0xffff0000, v99
	v_fmac_f32_e32 v127, v100, v100
	v_fmac_f32_e32 v127, v101, v101
	v_add_f32_e32 v79, v127, v79
	v_lshlrev_b64 v[66:67], 11, v[66:67]
	v_lshl_add_u64 v[130:131], v[68:69], 0, v[66:67]
	v_add_f32_dpp v79, v79, v79 quad_perm:[1,0,3,2] row_mask:0xf bank_mask:0xf bound_ctrl:1
	global_store_dwordx2 v[130:131], v[110:111], off
	global_store_dwordx2 v[130:131], v[106:107], off offset:512
	global_store_dwordx2 v[130:131], v[102:103], off offset:1024
	global_store_dwordx2 v[130:131], v[98:99], off offset:1536
	v_add_f32_dpp v79, v79, v79 quad_perm:[2,3,0,1] row_mask:0xf bank_mask:0xf bound_ctrl:1
	v_lshl_add_u64 v[66:67], v[76:77], 0, v[66:67]
	v_add_f32_dpp v79, v79, v79 row_half_mirror row_mask:0xf bank_mask:0xf bound_ctrl:1
	s_nop 1
	v_add_f32_dpp v79, v79, v79 row_mirror row_mask:0xf bank_mask:0xf bound_ctrl:1
	s_nop 0
	v_readlane_b32 s6, v79, 16
	v_readlane_b32 s2, v79, 0
	s_nop 0
	v_mov_b32_e32 v127, s6
	v_add_f32_e32 v127, s2, v127
	v_readlane_b32 s2, v79, 32
	s_nop 1
	v_add_f32_e32 v127, s2, v127
	v_readlane_b32 s2, v79, 48
	s_nop 1
	v_add_f32_e32 v79, s2, v127
	v_fmamk_f32 v79, v79, 0x3a800000, v117
	v_mul_f32_e32 v127, 0x4f800000, v79
	v_cmp_gt_f32_e32 vcc, s18, v79
	s_nop 1
	v_cndmask_b32_e32 v79, v79, v127, vcc
	v_sqrt_f32_e32 v127, v79
	s_nop 0
	v_add_u32_e32 v110, -1, v127
	v_fma_f32 v111, -v110, v127, v79
	v_cmp_ge_f32_e64 s[6:7], 0, v111
	v_add_u32_e32 v111, 1, v127
	s_nop 0
	v_cndmask_b32_e64 v110, v127, v110, s[6:7]
	v_fma_f32 v127, -v111, v127, v79
	v_cmp_lt_f32_e64 s[6:7], 0, v127
	v_mov_b32_e32 v127, v128
	s_nop 0
	v_cndmask_b32_e64 v110, v110, v111, s[6:7]
	v_mul_f32_e32 v111, 0x37800000, v110
	v_cndmask_b32_e32 v110, v110, v111, vcc
	v_cmp_class_f32_e32 vcc, v79, v118
	s_nop 1
	v_cndmask_b32_e32 v79, v110, v79, vcc
	v_div_scale_f32 v110, s[6:7], v79, v79, 1.0
	v_rcp_f32_e32 v111, v110
	s_nop 0
	v_fma_f32 v98, -v110, v111, 1.0
	v_fmac_f32_e32 v111, v98, v111
	v_div_scale_f32 v98, vcc, 1.0, v79, 1.0
	v_mul_f32_e32 v99, v98, v111
	v_fma_f32 v102, -v110, v99, v98
	v_fmac_f32_e32 v99, v102, v111
	v_fma_f32 v98, -v110, v99, v98
	v_div_fmas_f32 v98, v98, v111, v99
	v_div_fixup_f32 v98, v98, v79, 1.0
	v_pk_mul_f32 v[102:103], v[98:99], v[112:113] op_sel_hi:[0,1]
	v_pk_mul_f32 v[94:95], v[98:99], v[94:95] op_sel_hi:[0,1]
	v_pk_mul_f32 v[94:95], v[8:9], v[94:95]
	v_pk_mul_f32 v[102:103], v[10:11], v[102:103]
	v_pk_fma_f32 v[94:95], v[48:49], v[94:95], v[16:17]
	v_pk_fma_f32 v[102:103], v[50:51], v[102:103], v[18:19]
	v_cvt_pk_bf16_f32 v94, v94, v95
	v_cvt_pk_bf16_f32 v95, v102, v103
	global_store_dwordx2 v[66:67], v[94:95], off
	v_pk_mul_f32 v[94:95], v[98:99], v[108:109] op_sel_hi:[0,1]
	v_pk_mul_f32 v[92:93], v[98:99], v[92:93] op_sel_hi:[0,1]
	v_pk_mul_f32 v[92:93], v[0:1], v[92:93]
	v_pk_mul_f32 v[94:95], v[2:3], v[94:95]
	v_pk_fma_f32 v[92:93], v[52:53], v[92:93], v[20:21]
	v_pk_fma_f32 v[94:95], v[54:55], v[94:95], v[22:23]
	v_cvt_pk_bf16_f32 v92, v92, v93
	v_cvt_pk_bf16_f32 v93, v94, v95
	global_store_dwordx2 v[66:67], v[92:93], off offset:512
	v_pk_mul_f32 v[92:93], v[98:99], v[104:105] op_sel_hi:[0,1]
	v_pk_mul_f32 v[90:91], v[98:99], v[90:91] op_sel_hi:[0,1]
	v_pk_mul_f32 v[90:91], v[4:5], v[90:91]
	v_pk_mul_f32 v[92:93], v[6:7], v[92:93]
	v_pk_fma_f32 v[90:91], v[56:57], v[90:91], v[24:25]
	v_pk_fma_f32 v[92:93], v[58:59], v[92:93], v[26:27]
	v_cvt_pk_bf16_f32 v90, v90, v91
	v_cvt_pk_bf16_f32 v91, v92, v93
	global_store_dwordx2 v[66:67], v[90:91], off offset:1024
	v_pk_mul_f32 v[90:91], v[98:99], v[100:101] op_sel_hi:[0,1]
	v_pk_mul_f32 v[86:87], v[98:99], v[86:87] op_sel_hi:[0,1]
	v_pk_mul_f32 v[86:87], v[12:13], v[86:87]
	v_pk_mul_f32 v[90:91], v[14:15], v[90:91]
	v_pk_fma_f32 v[86:87], v[60:61], v[86:87], v[28:29]
	v_pk_fma_f32 v[90:91], v[62:63], v[90:91], v[30:31]
	v_cvt_pk_bf16_f32 v86, v86, v87
	v_cvt_pk_bf16_f32 v87, v90, v91
	global_store_dwordx2 v[66:67], v[86:87], off offset:1536
	s_waitcnt vmcnt(8)
	v_mov_b32_e32 v106, v125
	v_mov_b32_e32 v104, v124
	v_mov_b32_e32 v102, v123
	v_mov_b32_e32 v100, v122
	v_mov_b32_e32 v79, v121
	v_mov_b32_e32 v101, v120
	v_mov_b32_e32 v103, v119
	v_mov_b32_e32 v105, v81
	v_mov_b32_e32 v66, v80
	v_mov_b32_e32 v94, v96
	v_mov_b32_e32 v95, v97
	v_mov_b32_e32 v92, v88
	v_mov_b32_e32 v93, v89
	v_mov_b32_e32 v90, v84
	v_mov_b32_e32 v91, v85
	v_mov_b32_e32 v86, v82
	v_mov_b32_e32 v87, v83
	s_andn2_b64 exec, exec, s[4:5]
	s_cbranch_execz .LBB0_2141

.LBB0_2132:
	v_add_u32_e32 v98, 3, v66
	v_cmp_lt_i32_e64 s[6:7], v98, v114
	v_mov_b32_e32 v128, v115
	v_mov_b32_e32 v115, v116
	s_and_saveexec_b64 s[16:17], s[6:7]
	s_cbranch_execz .LBB0_2134
	v_ashrrev_i32_e32 v99, 31, v98
	v_lshlrev_b64 v[98:99], 6, v[98:99]
	v_lshl_add_u64 v[98:99], v[72:73], 0, v[98:99]
	global_load_dword v116, v[98:99], off

.LBB0_2135:
	s_or_b64 exec, exec, s[14:15]
	v_ashrrev_i32_e32 v67, 31, v66
	v_lshrrev_b32_e32 v98, 20, v67
	v_add_u32_e32 v98, v66, v98
	s_and_b64 s[6:7], exec, vcc
	v_ashrrev_i32_e32 v98, 12, v98
	v_cmp_gt_i32_e32 vcc, s13, v66
	s_or_b64 s[4:5], s[6:7], s[4:5]
	s_nop 0
	v_cndmask_b32_e32 v98, 8, v98, vcc
	v_cmp_ne_u32_e32 vcc, v98, v126
	s_and_saveexec_b64 s[6:7], vcc
	s_cbranch_execz .LBB0_2137
	v_add_u32_e32 v16, 18, v98
	v_mul_hi_i32_i24_e32 v17, 0x6000, v16
	v_mul_i32_i24_e32 v16, 0x6000, v16
	v_add_u32_e32 v32, 9, v98
	v_lshl_add_u64 v[28:29], v[74:75], 0, v[16:17]
	v_mul_hi_i32_i24_e32 v33, 0x6000, v32
	v_mul_i32_i24_e32 v32, 0x6000, v32
	v_add_co_u32_e32 v24, vcc, 0x1000, v28
	v_lshl_add_u64 v[32:33], s[8:9], 0, v[32:33]
	s_nop 0
	v_addc_co_u32_e32 v25, vcc, 0, v29, vcc
	v_lshl_add_u64 v[32:33], v[32:33], 0, v[64:65]
	v_add_co_u32_e32 v36, vcc, 0x5000, v32
	v_lshl_add_u64 v[44:45], v[32:33], 0, s[10:11]
	s_nop 0
	v_addc_co_u32_e32 v37, vcc, 0, v33, vcc
	global_load_dwordx4 v[48:51], v[24:25], off
	global_load_dwordx4 v[52:55], v[24:25], off offset:1024
	global_load_dwordx4 v[16:19], v[28:29], off
	global_load_dwordx4 v[20:23], v[28:29], off offset:1024
	global_load_dwordx4 v[56:59], v[24:25], off offset:2048
	global_load_dwordx4 v[60:63], v[24:25], off offset:3072
	s_nop 0
	global_load_dwordx4 v[24:27], v[28:29], off offset:2048
	s_nop 0
	global_load_dwordx4 v[28:31], v[28:29], off offset:3072
	s_nop 0
	global_load_dwordx4 v[32:35], v[44:45], off offset:1024
	global_load_dwordx4 v[40:43], v[44:45], off offset:2048
	s_nop 0
	global_load_dwordx4 v[36:39], v[36:37], off
	s_nop 0
	global_load_dwordx4 v[44:47], v[44:45], off offset:3072
	v_mov_b32_e32 v126, v98
	s_waitcnt vmcnt(11)
	v_pk_add_f32 v[50:51], v[50:51], 1.0 op_sel_hi:[1,0]
	v_pk_add_f32 v[48:49], v[48:49], 1.0 op_sel_hi:[1,0]
	s_waitcnt vmcnt(10)
	v_pk_add_f32 v[54:55], v[54:55], 1.0 op_sel_hi:[1,0]
	v_pk_add_f32 v[52:53], v[52:53], 1.0 op_sel_hi:[1,0]
	s_waitcnt vmcnt(7)
	v_pk_add_f32 v[58:59], v[58:59], 1.0 op_sel_hi:[1,0]
	v_pk_add_f32 v[56:57], v[56:57], 1.0 op_sel_hi:[1,0]
	s_waitcnt vmcnt(6)
	v_pk_add_f32 v[62:63], v[62:63], 1.0 op_sel_hi:[1,0]
	v_pk_add_f32 v[60:61], v[60:61], 1.0 op_sel_hi:[1,0]
	s_waitcnt vmcnt(0)

.LBB0_2193:
	s_or_b64 exec, exec, s[0:1]
	v_readlane_b32 s2, v242, 1
	s_waitcnt lgkmcnt(0)
	s_barrier
	s_nop 0
	s_mov_b32 s0, 0
	v_readlane_b32 s3, v242, 2
	s_load_dwordx4 s[8:11], s[2:3], s0 offset:0xe8
	s_load_dwordx2 s[6:7], s[2:3], s0 offset:0xf8
	s_load_dwordx2 s[4:5], s[2:3], s0 offset:0x108
	v_readlane_b32 s0, v242, 18
	v_mov_b32_e32 v140, v208
	v_readlane_b32 s1, v242, 19
	s_andn2_b64 vcc, exec, s[0:1]
	v_readfirstlane_b32 s33, v140
	s_cbranch_vccnz .LBB0_2205
	v_lshlrev_b32_e32 v0, 4, v140
	v_add_u32_e32 v1, 0x2000, v0
	v_ashrrev_i32_e32 v2, 31, v1
	v_lshrrev_b32_e32 v2, 22, v2
	v_add_u32_e32 v2, v1, v2
	v_ashrrev_i32_e32 v2, 10, v2
	v_mul_i32_i24_e32 v3, 0x400, v2
	v_sub_u32_e32 v1, v1, v3
	v_lshrrev_b32_e32 v3, 4, v1
	v_bitop3_b32 v1, v3, v1, 32 bitop3:0x6c
	v_ashrrev_i32_e32 v3, 31, v1
	v_lshrrev_b32_e32 v3, 26, v3
	v_add_u32_e32 v3, v1, v3
	v_lshlrev_b32_e32 v5, 3, v2
	v_ashrrev_i32_e32 v4, 6, v3
	v_and_b32_e32 v5, -16, v5
	v_and_b32_e32 v3, 0xc0, v3
	v_add_u32_e32 v5, v4, v5
	v_sub_u32_e32 v1, v1, v3
	v_mov_b32_e32 v3, 1
	v_and_b32_e32 v4, 3, v4
	s_mov_b32 s0, 0x1fffe0
	v_lshrrev_b32_e32 v6, 2, v5
	v_lshlrev_b32_e32 v7, 1, v5
	v_lshlrev_b32_e32 v2, 5, v2
	v_ashrrev_i16_sdwa v1, v3, sext(v1) dst_sel:DWORD dst_unused:UNUSED_PAD src0_sel:DWORD src1_sel:BYTE_0
	v_and_or_b32 v4, v5, s0, v4
	v_and_b32_e32 v6, 4, v6
	v_and_b32_e32 v7, 24, v7
	v_and_b32_e32 v2, 32, v2
	v_bfe_i32 v1, v1, 0, 16
	v_or3_b32 v4, v4, v6, v7
	v_add_lshl_u32 v1, v2, v1, 1
	v_lshl_add_u32 v128, v4, 11, v1
	v_lshl_add_u32 v130, v5, 11, v1
	v_bfe_i32 v1, v140, 27, 1
	v_lshrrev_b32_e32 v1, 22, v1
	v_add_u32_e32 v1, v0, v1
	v_and_b32_e32 v1, 0xfffffc00, v1
	v_sub_u32_e32 v0, v0, v1
	v_lshrrev_b32_e32 v1, 4, v0
	v_ashrrev_i32_e32 v4, 31, v140
	v_bitop3_b32 v0, v1, v0, 32 bitop3:0x6c
	v_lshrrev_b32_e32 v4, 26, v4
	v_ashrrev_i32_e32 v1, 31, v0
	v_add_u32_e32 v4, v140, v4
	s_waitcnt lgkmcnt(0)
	s_add_u32 s38, s4, 0xdbff000
	v_lshrrev_b32_e32 v1, 26, v1
	v_ashrrev_i32_e32 v4, 6, v4
	s_addc_u32 s39, s5, 0
	v_add_u32_e32 v1, v0, v1
	v_lshlrev_b32_e32 v5, 3, v4
	s_add_u32 s40, s4, 0x166f000
	v_ashrrev_i32_e32 v2, 6, v1
	v_and_b32_e32 v5, -16, v5
	v_readlane_b32 s2, v242, 0
	s_addc_u32 s41, s5, 0
	v_add_u32_e32 v5, v2, v5
	v_and_b32_e32 v2, 3, v2
	s_ashr_i32 s42, s2, 31
	v_and_or_b32 v2, v5, s0, v2
	s_lshr_b32 s0, s42, 29
	s_add_i32 s0, s2, s0
	s_ashr_i32 s15, s33, 6
	s_ashr_i32 s1, s0, 3
	s_and_b32 s0, s0, -8
	s_ashr_i32 s16, s33, 8
	s_lshl_b32 s17, s15, 10
	s_sub_i32 s0, s2, s0
	s_cmp_lt_i32 s0, 0
	s_movk_i32 s43, 0xde
	s_cselect_b32 s2, s43, 0xdd
	s_mul_i32 s0, s2, s0
	s_add_i32 s0, s0, s1
	s_mul_hi_i32 s1, s0, 0x4ec4ec4f
	s_lshr_b32 s2, s1, 31
	s_ashr_i32 s1, s1, 5
	s_add_i32 s1, s1, s2
	s_lshl_b32 s2, s1, 3
	s_mulk_i32 s1, 0x68
	s_sub_i32 s0, s0, s1
	s_bfe_i32 s1, s0, 0x80000
	s_bfe_u32 s1, s1, 0x3000c
	s_add_i32 s1, s0, s1
	s_bfe_i32 s3, s1, 0x80000
	s_and_b32 s1, s1, 0xf8
	s_sub_i32 s0, s0, s1
	s_sext_i32_i16 s3, s3
	s_sext_i32_i8 s0, s0
	s_lshr_b32 s14, s3, 3
	s_add_i32 s2, s2, s0
	v_and_b32_e32 v1, 0xc0, v1
	s_ashr_i32 s3, s2, 31
	s_bfe_i64 s[12:13], s[14:15], 0x100000
	v_sub_u32_e32 v0, v0, v1
	s_lshl_b64 s[0:1], s[2:3], 19
	s_lshl_b64 s[12:13], s[12:13], 19
	v_lshrrev_b32_e32 v6, 2, v5
	v_lshlrev_b32_e32 v7, 1, v5
	v_lshlrev_b32_e32 v4, 5, v4
	v_ashrrev_i16_sdwa v0, v3, sext(v0) dst_sel:DWORD dst_unused:UNUSED_PAD src0_sel:DWORD src1_sel:BYTE_0
	s_add_u32 s12, s40, s12
	v_and_b32_e32 v6, 4, v6
	v_and_b32_e32 v7, 24, v7
	v_and_b32_e32 v4, 32, v4
	v_bfe_i32 v0, v0, 0, 16
	s_addc_u32 s13, s41, s13
	s_add_i32 s3, s17, 0
	v_or3_b32 v2, v2, v6, v7
	v_add_lshl_u32 v0, v4, v0, 1
	s_add_i32 s44, s3, 0x10000
	v_lshl_add_u32 v132, v2, 11, v0
	v_lshl_add_u32 v134, v5, 11, v0
	v_mov_b32_e32 v0, 0x7f
	s_mov_b64 s[18:19], s[12:13]
	s_mov_b32 m0, s44
	s_add_i32 s45, s3, 0x12000
	v_mov_b32_e32 v133, 0
	global_load_lds_dwordx4 v132, s[18:19]
	s_mov_b32 m0, s45
	s_mov_b32 s51, 0
	global_load_lds_dwordx4 v128, s[18:19]
	s_add_u32 s18, s38, s0
	s_addc_u32 s19, s39, s1
	s_mov_b64 s[0:1], s[18:19]
	s_mov_b32 m0, s3
	s_add_i32 s46, s3, 0x2000
	v_mov_b32_e32 v129, v133
	global_load_lds_dwordx4 v134, s[0:1]
	s_mov_b32 m0, s46
	v_mov_b32_e32 v135, v133
	global_load_lds_dwordx4 v130, s[0:1]
	s_add_u32 s0, s12, 0x40000
	s_addc_u32 s1, s13, 0
	s_add_i32 s47, s3, 0x14000
	s_mov_b32 m0, s47
	s_add_i32 s48, s3, 0x16000
	v_mov_b32_e32 v131, v133
	global_load_lds_dwordx4 v132, s[0:1]
	s_mov_b32 m0, s48
	s_nop 0
	global_load_lds_dwordx4 v128, s[0:1]
	s_add_u32 s0, s18, 0x40000
	s_addc_u32 s1, s19, 0
	s_add_i32 s49, s3, 0x4000
	s_mov_b32 m0, s49
	s_add_i32 s50, s3, 0x6000
	s_cmp_lg_u32 s16, 1
	global_load_lds_dwordx4 v134, s[0:1]
	s_mov_b32 m0, s50
	s_nop 0
	global_load_lds_dwordx4 v130, s[0:1]
	s_cbranch_scc1 .LBB0_2196
	s_barrier

.LBB0_3095:
	v_lshlrev_b32_e32 v130, 16, v92
	v_and_b32_e32 v131, 0xffff0000, v92
	v_lshlrev_b32_e32 v132, 16, v90
	v_and_b32_e32 v133, 0xffff0000, v90
	v_lshlrev_b32_e32 v92, 16, v93
	v_and_b32_e32 v93, 0xffff0000, v93
	v_lshlrev_b32_e32 v90, 16, v91
	v_and_b32_e32 v91, 0xffff0000, v91
	v_pk_fma_f32 v[110:111], v[36:37], v[110:111], v[130:131]
	v_pk_fma_f32 v[106:107], v[32:33], v[106:107], v[132:133]
	v_pk_fma_f32 v[92:93], v[38:39], v[112:113], v[92:93]
	v_cvt_pk_bf16_f32 v110, v110, v111
	v_pk_fma_f32 v[90:91], v[34:35], v[108:109], v[90:91]
	v_cvt_pk_bf16_f32 v106, v106, v107
	v_cvt_pk_bf16_f32 v111, v92, v93
	v_and_b32_e32 v93, 0xffff0000, v110
	v_cvt_pk_bf16_f32 v107, v90, v91
	v_and_b32_e32 v91, 0xffff0000, v106
	v_lshlrev_b32_e32 v134, 16, v88
	v_and_b32_e32 v135, 0xffff0000, v88
	v_lshlrev_b32_e32 v92, 16, v110
	v_lshlrev_b32_e32 v90, 16, v106
	v_mul_f32_e32 v79, v93, v93
	v_mul_f32_e32 v127, v91, v91
	v_lshlrev_b32_e32 v88, 16, v89
	v_and_b32_e32 v89, 0xffff0000, v89
	v_lshlrev_b32_e32 v112, 16, v111
	v_lshlrev_b32_e32 v108, 16, v107
	v_pk_fma_f32 v[102:103], v[40:41], v[102:103], v[134:135]
	v_fmac_f32_e32 v79, v92, v92
	v_fmac_f32_e32 v127, v90, v90
	v_and_b32_e32 v113, 0xffff0000, v111
	v_and_b32_e32 v109, 0xffff0000, v107
	v_pk_fma_f32 v[88:89], v[42:43], v[104:105], v[88:89]
	v_cvt_pk_bf16_f32 v102, v102, v103
	v_fmac_f32_e32 v79, v112, v112
	v_fmac_f32_e32 v127, v108, v108
	v_cvt_pk_bf16_f32 v103, v88, v89
	v_and_b32_e32 v89, 0xffff0000, v102
	v_fmac_f32_e32 v79, v113, v113
	v_fmac_f32_e32 v127, v109, v109
	v_lshlrev_b32_e32 v136, 16, v84
	v_and_b32_e32 v137, 0xffff0000, v84
	v_lshlrev_b32_e32 v88, 16, v102
	v_add_f32_e32 v79, v127, v79
	v_mul_f32_e32 v127, v89, v89
	v_lshlrev_b32_e32 v84, 16, v85
	v_and_b32_e32 v85, 0xffff0000, v85
	v_lshlrev_b32_e32 v104, 16, v103
	v_pk_fma_f32 v[98:99], v[44:45], v[98:99], v[136:137]
	v_fmac_f32_e32 v127, v88, v88
	v_and_b32_e32 v105, 0xffff0000, v103
	v_pk_fma_f32 v[84:85], v[46:47], v[100:101], v[84:85]
	v_cvt_pk_bf16_f32 v98, v98, v99
	v_fmac_f32_e32 v127, v104, v104
	v_cvt_pk_bf16_f32 v99, v84, v85
	v_and_b32_e32 v85, 0xffff0000, v98
	v_fmac_f32_e32 v127, v105, v105
	v_lshlrev_b32_e32 v84, 16, v98
	v_add_f32_e32 v79, v127, v79
	v_mul_f32_e32 v127, v85, v85
	v_lshlrev_b32_e32 v100, 16, v99
	v_fmac_f32_e32 v127, v84, v84
	v_and_b32_e32 v101, 0xffff0000, v99
	v_fmac_f32_e32 v127, v100, v100
	v_fmac_f32_e32 v127, v101, v101
	v_add_f32_e32 v79, v127, v79
	v_lshlrev_b64 v[66:67], 11, v[66:67]
	v_lshl_add_u64 v[130:131], v[68:69], 0, v[66:67]
	v_add_f32_dpp v79, v79, v79 quad_perm:[1,0,3,2] row_mask:0xf bank_mask:0xf bound_ctrl:1
	global_store_dwordx2 v[130:131], v[110:111], off
	global_store_dwordx2 v[130:131], v[106:107], off offset:512
	global_store_dwordx2 v[130:131], v[102:103], off offset:1024
	global_store_dwordx2 v[130:131], v[98:99], off offset:1536
	v_add_f32_dpp v79, v79, v79 quad_perm:[2,3,0,1] row_mask:0xf bank_mask:0xf bound_ctrl:1
	v_lshl_add_u64 v[66:67], v[76:77], 0, v[66:67]
	v_add_f32_dpp v79, v79, v79 row_half_mirror row_mask:0xf bank_mask:0xf bound_ctrl:1
	s_nop 1
	v_add_f32_dpp v79, v79, v79 row_mirror row_mask:0xf bank_mask:0xf bound_ctrl:1
	s_nop 0
	v_readlane_b32 s6, v79, 16
	v_readlane_b32 s2, v79, 0
	s_nop 0
	v_mov_b32_e32 v127, s6
	v_add_f32_e32 v127, s2, v127
	v_readlane_b32 s2, v79, 32
	s_nop 1
	v_add_f32_e32 v127, s2, v127
	v_readlane_b32 s2, v79, 48
	s_nop 1
	v_add_f32_e32 v79, s2, v127
	v_fmamk_f32 v79, v79, 0x3a800000, v117
	v_mul_f32_e32 v127, 0x4f800000, v79
	v_cmp_gt_f32_e32 vcc, s18, v79
	s_nop 1
	v_cndmask_b32_e32 v79, v79, v127, vcc
	v_sqrt_f32_e32 v127, v79
	s_nop 0
	v_add_u32_e32 v110, -1, v127
	v_fma_f32 v111, -v110, v127, v79
	v_cmp_ge_f32_e64 s[6:7], 0, v111
	v_add_u32_e32 v111, 1, v127
	s_nop 0
	v_cndmask_b32_e64 v110, v127, v110, s[6:7]
	v_fma_f32 v127, -v111, v127, v79
	v_cmp_lt_f32_e64 s[6:7], 0, v127
	v_mov_b32_e32 v127, v128
	s_nop 0
	v_cndmask_b32_e64 v110, v110, v111, s[6:7]
	v_mul_f32_e32 v111, 0x37800000, v110
	v_cndmask_b32_e32 v110, v110, v111, vcc
	v_cmp_class_f32_e32 vcc, v79, v118
	s_nop 1
	v_cndmask_b32_e32 v79, v110, v79, vcc
	v_div_scale_f32 v110, s[6:7], v79, v79, 1.0
	v_rcp_f32_e32 v111, v110
	s_nop 0
	v_fma_f32 v98, -v110, v111, 1.0
	v_fmac_f32_e32 v111, v98, v111
	v_div_scale_f32 v98, vcc, 1.0, v79, 1.0
	v_mul_f32_e32 v99, v98, v111
	v_fma_f32 v102, -v110, v99, v98
	v_fmac_f32_e32 v99, v102, v111
	v_fma_f32 v98, -v110, v99, v98
	v_div_fmas_f32 v98, v98, v111, v99
	v_div_fixup_f32 v98, v98, v79, 1.0
	v_pk_mul_f32 v[102:103], v[98:99], v[112:113] op_sel_hi:[0,1]
	v_pk_mul_f32 v[92:93], v[98:99], v[92:93] op_sel_hi:[0,1]
	v_pk_mul_f32 v[92:93], v[8:9], v[92:93]
	v_pk_mul_f32 v[102:103], v[10:11], v[102:103]
	v_pk_fma_f32 v[92:93], v[48:49], v[92:93], v[16:17]
	v_pk_fma_f32 v[102:103], v[50:51], v[102:103], v[18:19]
	v_cvt_pk_bf16_f32 v92, v92, v93
	v_cvt_pk_bf16_f32 v93, v102, v103
	global_store_dwordx2 v[66:67], v[92:93], off
	v_pk_mul_f32 v[92:93], v[98:99], v[108:109] op_sel_hi:[0,1]
	v_pk_mul_f32 v[90:91], v[98:99], v[90:91] op_sel_hi:[0,1]
	v_pk_mul_f32 v[90:91], v[0:1], v[90:91]
	v_pk_mul_f32 v[92:93], v[2:3], v[92:93]
	v_pk_fma_f32 v[90:91], v[52:53], v[90:91], v[20:21]
	v_pk_fma_f32 v[92:93], v[54:55], v[92:93], v[22:23]
	v_cvt_pk_bf16_f32 v90, v90, v91
	v_cvt_pk_bf16_f32 v91, v92, v93
	global_store_dwordx2 v[66:67], v[90:91], off offset:512
	v_pk_mul_f32 v[90:91], v[98:99], v[104:105] op_sel_hi:[0,1]
	v_pk_mul_f32 v[88:89], v[98:99], v[88:89] op_sel_hi:[0,1]
	v_pk_mul_f32 v[88:89], v[4:5], v[88:89]
	v_pk_mul_f32 v[90:91], v[6:7], v[90:91]
	v_pk_fma_f32 v[88:89], v[56:57], v[88:89], v[24:25]
	v_pk_fma_f32 v[90:91], v[58:59], v[90:91], v[26:27]
	v_cvt_pk_bf16_f32 v88, v88, v89
	v_cvt_pk_bf16_f32 v89, v90, v91
	global_store_dwordx2 v[66:67], v[88:89], off offset:1024
	v_pk_mul_f32 v[88:89], v[98:99], v[100:101] op_sel_hi:[0,1]
	v_pk_mul_f32 v[84:85], v[98:99], v[84:85] op_sel_hi:[0,1]
	v_pk_mul_f32 v[84:85], v[12:13], v[84:85]
	v_pk_mul_f32 v[88:89], v[14:15], v[88:89]
	v_pk_fma_f32 v[84:85], v[60:61], v[84:85], v[28:29]
	v_pk_fma_f32 v[88:89], v[62:63], v[88:89], v[30:31]
	v_cvt_pk_bf16_f32 v84, v84, v85
	v_cvt_pk_bf16_f32 v85, v88, v89
	global_store_dwordx2 v[66:67], v[84:85], off offset:1536
	s_waitcnt vmcnt(8)
	v_mov_b32_e32 v106, v125
	v_mov_b32_e32 v104, v124
	v_mov_b32_e32 v102, v123
	v_mov_b32_e32 v100, v122
	v_mov_b32_e32 v79, v121
	v_mov_b32_e32 v101, v120
	v_mov_b32_e32 v103, v119
	v_mov_b32_e32 v105, v81
	v_mov_b32_e32 v66, v80
	v_mov_b32_e32 v92, v96
	v_mov_b32_e32 v93, v97
	v_mov_b32_e32 v90, v94
	v_mov_b32_e32 v91, v95
	v_mov_b32_e32 v88, v86
	v_mov_b32_e32 v89, v87
	v_mov_b32_e32 v84, v82
	v_mov_b32_e32 v85, v83
	s_andn2_b64 exec, exec, s[4:5]
	s_cbranch_execz .LBB0_3109

.LBB0_3103:
	s_or_b64 exec, exec, s[14:15]
	v_ashrrev_i32_e32 v67, 31, v66
	v_lshrrev_b32_e32 v98, 20, v67
	v_add_u32_e32 v98, v66, v98
	s_and_b64 s[6:7], exec, vcc
	v_ashrrev_i32_e32 v98, 12, v98
	v_cmp_gt_i32_e32 vcc, s13, v66
	s_or_b64 s[4:5], s[6:7], s[4:5]
	s_nop 0
	v_cndmask_b32_e32 v98, 8, v98, vcc
	v_cmp_ne_u32_e32 vcc, v98, v126
	s_and_saveexec_b64 s[6:7], vcc
	s_cbranch_execz .LBB0_3105
	v_add_u32_e32 v16, 27, v98
	v_mul_hi_i32_i24_e32 v17, 0x6000, v16
	v_mul_i32_i24_e32 v16, 0x6000, v16
	v_lshl_add_u64 v[32:33], v[74:75], 0, v[16:17]
	v_add_co_u32_e32 v34, vcc, 0x1000, v32
	v_mov_b32_e32 v126, v98
	s_nop 0
	v_addc_co_u32_e32 v35, vcc, 0, v33, vcc
	global_load_dwordx4 v[48:51], v[34:35], off
	global_load_dwordx4 v[52:55], v[34:35], off offset:1024
	global_load_dwordx4 v[16:19], v[32:33], off
	global_load_dwordx4 v[20:23], v[32:33], off offset:1024
	global_load_dwordx4 v[56:59], v[34:35], off offset:2048
	global_load_dwordx4 v[60:63], v[34:35], off offset:3072
	global_load_dwordx4 v[24:27], v[32:33], off offset:2048
	global_load_dwordx4 v[28:31], v[32:33], off offset:3072
	v_add_u32_e32 v32, 18, v98
	v_mul_hi_i32_i24_e32 v33, 0x6000, v32
	v_mul_i32_i24_e32 v32, 0x6000, v32
	v_lshl_add_u64 v[32:33], s[8:9], 0, v[32:33]
	v_lshl_add_u64 v[32:33], v[32:33], 0, v[64:65]
	v_lshl_add_u64 v[108:109], v[32:33], 0, s[10:11]
	v_add_co_u32_e32 v110, vcc, 0x5000, v32
	s_waitcnt vmcnt(7)
	v_pk_add_f32 v[50:51], v[50:51], 1.0 op_sel_hi:[1,0]
	v_addc_co_u32_e32 v111, vcc, 0, v33, vcc
	global_load_dwordx4 v[32:35], v[108:109], off offset:1024
	global_load_dwordx4 v[40:43], v[108:109], off offset:2048
	global_load_dwordx4 v[36:39], v[110:111], off
	global_load_dwordx4 v[44:47], v[108:109], off offset:3072
	v_pk_add_f32 v[48:49], v[48:49], 1.0 op_sel_hi:[1,0]
	s_waitcnt vmcnt(10)
	v_pk_add_f32 v[54:55], v[54:55], 1.0 op_sel_hi:[1,0]
	v_pk_add_f32 v[52:53], v[52:53], 1.0 op_sel_hi:[1,0]
	s_waitcnt vmcnt(7)
	v_pk_add_f32 v[58:59], v[58:59], 1.0 op_sel_hi:[1,0]
	v_pk_add_f32 v[56:57], v[56:57], 1.0 op_sel_hi:[1,0]
	s_waitcnt vmcnt(6)
	v_pk_add_f32 v[62:63], v[62:63], 1.0 op_sel_hi:[1,0]
	v_pk_add_f32 v[60:61], v[60:61], 1.0 op_sel_hi:[1,0]
	s_waitcnt vmcnt(0)

.LBB0_4047:
	v_lshlrev_b32_e32 v96, 16, v52
	v_and_b32_e32 v97, 0xffff0000, v52
	v_lshlrev_b32_e32 v98, 16, v50
	v_and_b32_e32 v99, 0xffff0000, v50
	v_lshlrev_b32_e32 v102, 16, v46
	v_and_b32_e32 v103, 0xffff0000, v46
	v_lshlrev_b32_e32 v46, 16, v47
	v_and_b32_e32 v47, 0xffff0000, v47
	v_pk_fma_f32 v[76:77], v[20:21], v[76:77], v[96:97]
	v_pk_fma_f32 v[72:73], v[16:17], v[72:73], v[98:99]
	v_lshlrev_b32_e32 v52, 16, v53
	v_and_b32_e32 v53, 0xffff0000, v53
	v_lshlrev_b32_e32 v50, 16, v51
	v_and_b32_e32 v51, 0xffff0000, v51
	v_pk_fma_f32 v[66:67], v[30:31], v[66:67], v[46:47]
	v_mul_f32_e32 v45, v77, v77
	v_mul_f32_e32 v46, v73, v73
	v_pk_fma_f32 v[52:53], v[22:23], v[78:79], v[52:53]
	v_pk_fma_f32 v[50:51], v[18:19], v[74:75], v[50:51]
	v_fmac_f32_e32 v45, v76, v76
	v_fmac_f32_e32 v46, v72, v72
	v_lshlrev_b32_e32 v100, 16, v48
	v_and_b32_e32 v101, 0xffff0000, v48
	v_fmac_f32_e32 v45, v52, v52
	v_fmac_f32_e32 v46, v50, v50
	v_pk_fma_f32 v[68:69], v[24:25], v[68:69], v[100:101]
	v_fmac_f32_e32 v45, v53, v53
	v_fmac_f32_e32 v46, v51, v51
	v_lshlrev_b32_e32 v48, 16, v49
	v_and_b32_e32 v49, 0xffff0000, v49
	v_add_f32_e32 v45, v45, v46
	v_mul_f32_e32 v46, v69, v69
	v_pk_fma_f32 v[70:71], v[26:27], v[70:71], v[48:49]
	v_fmac_f32_e32 v46, v68, v68
	v_fmac_f32_e32 v46, v70, v70
	v_pk_fma_f32 v[64:65], v[28:29], v[64:65], v[102:103]
	v_fmac_f32_e32 v46, v71, v71
	v_add_f32_e32 v45, v46, v45
	v_mul_f32_e32 v46, v65, v65
	v_fmac_f32_e32 v46, v64, v64
	v_fmac_f32_e32 v46, v66, v66
	v_fmac_f32_e32 v46, v67, v67
	v_add_f32_e32 v45, v46, v45
	v_lshlrev_b64 v[32:33], 12, v[32:33]
	v_lshl_add_u64 v[32:33], v[42:43], 0, v[32:33]
	v_add_f32_dpp v45, v45, v45 quad_perm:[1,0,3,2] row_mask:0xf bank_mask:0xf bound_ctrl:1
	v_mov_b32_e32 v86, v94
	s_nop 0
	v_add_f32_dpp v45, v45, v45 quad_perm:[2,3,0,1] row_mask:0xf bank_mask:0xf bound_ctrl:1
	s_nop 1
	v_add_f32_dpp v45, v45, v45 row_half_mirror row_mask:0xf bank_mask:0xf bound_ctrl:1
	s_nop 1
	v_add_f32_dpp v45, v45, v45 row_mirror row_mask:0xf bank_mask:0xf bound_ctrl:1
	s_nop 0
	v_readlane_b32 s1, v45, 16
	v_readlane_b32 s0, v45, 0
	s_nop 0
	v_mov_b32_e32 v46, s1
	v_add_f32_e32 v46, s0, v46
	v_readlane_b32 s0, v45, 32
	s_nop 1
	v_add_f32_e32 v46, s0, v46
	v_readlane_b32 s0, v45, 48
	s_nop 1
	v_add_f32_e32 v45, s0, v46
	v_fmamk_f32 v45, v45, 0x3a800000, v83
	v_mul_f32_e32 v46, 0x4f800000, v45
	v_cmp_gt_f32_e32 vcc, s13, v45
	s_nop 1
	v_cndmask_b32_e32 v45, v45, v46, vcc
	v_sqrt_f32_e32 v46, v45
	s_nop 0
	v_add_u32_e32 v47, -1, v46
	v_fma_f32 v48, -v47, v46, v45
	v_cmp_ge_f32_e64 s[0:1], 0, v48
	v_add_u32_e32 v48, 1, v46
	s_nop 0
	v_cndmask_b32_e64 v47, v46, v47, s[0:1]
	v_fma_f32 v46, -v48, v46, v45
	v_cmp_lt_f32_e64 s[0:1], 0, v46
	s_nop 1
	v_cndmask_b32_e64 v46, v47, v48, s[0:1]
	v_mul_f32_e32 v47, 0x37800000, v46
	v_cndmask_b32_e32 v46, v46, v47, vcc
	v_cmp_class_f32_e32 vcc, v45, v84
	s_nop 1
	v_cndmask_b32_e32 v45, v46, v45, vcc
	v_div_scale_f32 v46, s[0:1], v45, v45, 1.0
	v_rcp_f32_e32 v47, v46
	s_nop 0
	v_fma_f32 v48, -v46, v47, 1.0
	v_fmac_f32_e32 v47, v48, v47
	v_div_scale_f32 v48, vcc, 1.0, v45, 1.0
	v_mul_f32_e32 v49, v48, v47
	v_fma_f32 v74, -v46, v49, v48
	v_fmac_f32_e32 v49, v74, v47
	v_fma_f32 v46, -v46, v49, v48
	v_div_fmas_f32 v46, v46, v47, v49
	v_div_fixup_f32 v74, v46, v45, 1.0
	v_pk_mul_f32 v[46:47], v[76:77], v[74:75] op_sel_hi:[1,0]
	v_pk_mul_f32 v[48:49], v[52:53], v[74:75] op_sel_hi:[1,0]
	v_pk_mul_f32 v[46:47], v[0:1], v[46:47]
	v_pk_mul_f32 v[48:49], v[2:3], v[48:49]
	global_store_dwordx4 v[32:33], v[46:49], off
	s_nop 0
	s_nop 0
	v_pk_mul_f32 v[46:47], v[72:73], v[74:75] op_sel_hi:[1,0]
	v_pk_mul_f32 v[48:49], v[50:51], v[74:75] op_sel_hi:[1,0]
	v_pk_mul_f32 v[46:47], v[4:5], v[46:47]
	v_pk_mul_f32 v[48:49], v[6:7], v[48:49]
	global_store_dwordx4 v[32:33], v[46:49], off offset:1024
	s_nop 0
	s_nop 0
	v_pk_mul_f32 v[46:47], v[68:69], v[74:75] op_sel_hi:[1,0]
	v_pk_mul_f32 v[48:49], v[70:71], v[74:75] op_sel_hi:[1,0]
	v_pk_mul_f32 v[46:47], v[8:9], v[46:47]
	v_pk_mul_f32 v[48:49], v[10:11], v[48:49]
	global_store_dwordx4 v[32:33], v[46:49], off offset:2048
	s_nop 0
	s_nop 0
	v_pk_mul_f32 v[46:47], v[64:65], v[74:75] op_sel_hi:[1,0]
	v_pk_mul_f32 v[48:49], v[66:67], v[74:75] op_sel_hi:[1,0]
	v_pk_mul_f32 v[46:47], v[12:13], v[46:47]
	v_pk_mul_f32 v[48:49], v[14:15], v[48:49]
	global_store_dwordx4 v[32:33], v[46:49], off offset:3072
	s_waitcnt vmcnt(4)
	v_mov_b32_e32 v45, v89
	v_mov_b32_e32 v52, v62
	v_mov_b32_e32 v72, v90
	v_mov_b32_e32 v53, v63
	v_mov_b32_e32 v68, v92
	v_mov_b32_e32 v70, v91
	v_mov_b32_e32 v66, v93
	v_mov_b32_e32 v67, v88
	v_mov_b32_e32 v69, v87
	v_mov_b32_e32 v71, v55
	v_mov_b32_e32 v32, v54
	v_mov_b32_e32 v50, v60
	v_mov_b32_e32 v51, v61
	v_mov_b32_e32 v48, v58
	v_mov_b32_e32 v49, v59
	v_mov_b32_e32 v46, v56
	v_mov_b32_e32 v47, v57
	s_andn2_b64 exec, exec, s[10:11]
	s_cbranch_execz .LBB0_4061

.LBB0_4052:
	v_add_u32_e32 v64, 3, v32
	v_cmp_lt_i32_e64 s[0:1], v64, v80
	v_mov_b32_e32 v94, v81
	v_mov_b32_e32 v81, v82
	s_and_saveexec_b64 s[16:17], s[0:1]
	s_cbranch_execz .LBB0_4054
	v_ashrrev_i32_e32 v65, 31, v64
	v_lshlrev_b64 v[64:65], 6, v[64:65]
	v_lshl_add_u64 v[64:65], v[40:41], 0, v[64:65]
	global_load_dword v82, v[64:65], off

.LBB0_4055:
	s_or_b64 exec, exec, s[14:15]
	v_ashrrev_i32_e32 v33, 31, v32
	v_lshrrev_b32_e32 v64, 20, v33
	v_add_u32_e32 v64, v32, v64
	s_and_b64 s[0:1], exec, vcc
	v_ashrrev_i32_e32 v64, 12, v64
	s_or_b64 s[10:11], s[0:1], s[10:11]
	v_cmp_ne_u32_e32 vcc, v64, v85
	s_and_saveexec_b64 s[0:1], vcc
	s_cbranch_execz .LBB0_4057
	v_add_u32_e32 v16, 27, v64
	v_mul_hi_i32_i24_e32 v17, 0x6000, v16
	v_mul_i32_i24_e32 v16, 0x6000, v16
	v_lshl_add_u64 v[16:17], s[6:7], 0, v[16:17]
	v_lshl_add_u64 v[16:17], v[16:17], 0, v[34:35]
	v_lshl_add_u64 v[74:75], v[16:17], 0, s[4:5]
	v_add_co_u32_e32 v76, vcc, 0x9000, v16
	v_mov_b32_e32 v85, v64
	s_nop 0
	v_addc_co_u32_e32 v77, vcc, 0, v17, vcc
	global_load_dwordx4 v[16:19], v[74:75], off offset:1024
	global_load_dwordx4 v[24:27], v[74:75], off offset:2048
	global_load_dwordx4 v[20:23], v[76:77], off
	global_load_dwordx4 v[28:31], v[74:75], off offset:3072
	s_waitcnt vmcnt(0)
